# prologue fp4 table conversion loop software-pipelined: next row loaded into a second register set while the current row is converted
# speedup vs baseline: 1.0058x; 1.0058x over previous
; __device__ __forceinline__ void row_to_fp4(const float* src, unsigned char* dst, size_t slice_stride, unsigned short* scale_out, int lane) {
;     f32x4 v[8]; float mx = 0.f;
; #pragma unroll
;     for (int q = 0; q < 8; ++q) { v[q] = ld_f4(src + q * 256 + lane * 4);
; __device__ __forceinline__ void p0_prologue(const Frame& F) {
;     ...
;     {
;         unsigned char* UB = (unsigned char*)(F.ws + WS_UB); unsigned char* VB = (unsigned char*)(F.ws + WS_VB);
;         unsigned short* SUV = (unsigned short*)(F.ws + WS_SU);
;         const int nrows = DEPTH * NEXP;
;         for (int r = F.gw; r < 2 * nrows; r += F.ngw) {
;             const bool isv = r >= nrows; const int rr = isv ? r - nrows : r;
;             row_to_fp4((isv ? F.peer_v : F.peer_u) + (size_t)rr * D, (isv ? VB : UB) + (size_t)(rr / NEXP) * NEXP * (D / 2) + (size_t)(rr % NEXP) * 128, (size_t)NEXP * 128, SUV + 2 * (size_t)rr + (isv ? 1 : 0), lane);
;         }
.LBB0_144:
	s_cmp_gt_i32 s94, 0x1ffff
	s_cbranch_scc1 .LBB0_151
	s_add_u32 s10, s62, 0x43400000
	v_lshlrev_b32_e32 v36, 1, v32
	s_addc_u32 s11, s63, 0
	v_ashrrev_i32_e32 v35, 31, v34
	v_ashrrev_i32_e32 v37, 31, v36
	v_cmp_eq_u32_e64 s[0:1], 0, v32
	s_movk_i32 s12, 0x1000
	s_movk_i32 s13, 0x7fff
	s_mov_b32 s14, 0x3f400000
	s_mov_b32 s15, 0x200000
	s_mov_b32 s16, 0x400000
	s_mov_b32 s17, 0x600000
	s_mov_b32 s18, 0x800000
	s_mov_b32 s19, 0xa00000
	s_mov_b32 s20, 0xc00000
	s_mov_b32 s21, s94
	s_mov_b32 s100, s21
	s_add_i32 s8, s100, 0xffff0000
	s_cmp_gt_i32 s100, 0xffff
	s_cselect_b32 s100, s8, s100
	s_cselect_b32 s22, s59, s57
	s_cselect_b32 s23, s58, s56
	s_ashr_i32 s101, s100, 31
	s_lshl_b64 s[100:101], s[100:101], 13
	s_add_u32 s8, s23, s100
	s_addc_u32 s9, s22, s101
	v_lshl_add_u64 v[132:133], v[34:35], 2, s[8:9]
	global_load_dwordx4 v[100:103], v[132:133], off
	global_load_dwordx4 v[104:107], v[132:133], off offset:1024
	global_load_dwordx4 v[108:111], v[132:133], off offset:2048
	global_load_dwordx4 v[112:115], v[132:133], off offset:3072
	v_add_co_u32_e32 v132, vcc, s12, v132
	s_nop 1
	v_addc_co_u32_e32 v133, vcc, 0, v133, vcc
	global_load_dwordx4 v[116:119], v[132:133], off
	global_load_dwordx4 v[120:123], v[132:133], off offset:1024
	global_load_dwordx4 v[124:127], v[132:133], off offset:2048
	global_load_dwordx4 v[128:131], v[132:133], off offset:3072
	s_branch .LBB0_147

; __device__ __forceinline__ void row_to_fp4(const float* src, unsigned char* dst, size_t slice_stride, unsigned short* scale_out, int lane) {
;     f32x4 v[8]; float mx = 0.f;
; #pragma unroll
;     for (int q = 0; q < 8; ++q) { v[q] = ld_f4(src + q * 256 + lane * 4);
;         mx = fmaxf(mx, fmaxf(fmaxf(__builtin_fabsf(v[q][0]), __builtin_fabsf(v[q][1])), fmaxf(__builtin_fabsf(v[q][2]), __builtin_fabsf(v[q][3])))); }
; #pragma unroll
;     for (int o = 1; o < 64; o <<= 1) mx = fmaxf(mx, __shfl_xor(mx, o));
; __device__ __forceinline__ void p0_prologue(const Frame& F) {
;     ...
;         for (int r = F.gw; r < 2 * nrows; r += F.ngw) {
;             const bool isv = r >= nrows; const int rr = isv ? r - nrows : r;
;             row_to_fp4((isv ? F.peer_v : F.peer_u) + (size_t)rr * D, (isv ? VB : UB) + (size_t)(rr / NEXP) * NEXP * (D / 2) + (size_t)(rr % NEXP) * 128, (size_t)NEXP * 128, SUV + 2 * (size_t)rr + (isv ? 1 : 0), lane);
.LBB0_147:
	s_add_i32 s8, s21, 0xffff0000
	s_cmp_gt_i32 s21, 0xffff
	s_cselect_b64 s[2:3], -1, 0
	s_and_b64 s[6:7], s[2:3], exec
	s_cselect_b32 s6, s8, s21
	s_cselect_b32 s22, s59, s57
	s_cselect_b32 s23, s58, s56
	s_ashr_i32 s7, s6, 31
	s_lshl_b64 s[8:9], s[6:7], 13
	s_add_u32 s8, s23, s8
	s_addc_u32 s9, s22, s9
	v_lshl_add_u64 v[0:1], v[34:35], 2, s[8:9]
	s_waitcnt vmcnt(0)
	v_mov_b32_e32 v28, v100
	v_mov_b32_e32 v29, v101
	v_mov_b32_e32 v30, v102
	v_mov_b32_e32 v31, v103
	v_mov_b32_e32 v24, v104
	v_mov_b32_e32 v25, v105
	v_mov_b32_e32 v26, v106
	v_mov_b32_e32 v27, v107
	v_mov_b32_e32 v20, v108
	v_mov_b32_e32 v21, v109
	v_mov_b32_e32 v22, v110
	v_mov_b32_e32 v23, v111
	v_mov_b32_e32 v16, v112
	v_mov_b32_e32 v17, v113
	v_mov_b32_e32 v18, v114
	v_mov_b32_e32 v19, v115
	v_mov_b32_e32 v12, v116
	v_mov_b32_e32 v13, v117
	v_mov_b32_e32 v14, v118
	v_mov_b32_e32 v15, v119
	v_mov_b32_e32 v8, v120
	v_mov_b32_e32 v9, v121
	v_mov_b32_e32 v10, v122
	v_mov_b32_e32 v11, v123
	v_mov_b32_e32 v4, v124
	v_mov_b32_e32 v5, v125
	v_mov_b32_e32 v6, v126
	v_mov_b32_e32 v7, v127
	v_mov_b32_e32 v0, v128
	v_mov_b32_e32 v1, v129
	v_mov_b32_e32 v2, v130
	v_mov_b32_e32 v3, v131
	s_add_i32 s100, s21, s82
	s_cmp_gt_i32 s100, 0x1ffff
	s_cselect_b32 s100, s21, s100
	s_add_i32 s8, s100, 0xffff0000
	s_cmp_gt_i32 s100, 0xffff
	s_cselect_b32 s100, s8, s100
	s_cselect_b32 s22, s59, s57
	s_cselect_b32 s23, s58, s56
	s_ashr_i32 s101, s100, 31
	s_lshl_b64 s[100:101], s[100:101], 13
	s_add_u32 s8, s23, s100
	s_addc_u32 s9, s22, s101
	v_lshl_add_u64 v[132:133], v[34:35], 2, s[8:9]
	global_load_dwordx4 v[100:103], v[132:133], off
	global_load_dwordx4 v[104:107], v[132:133], off offset:1024
	global_load_dwordx4 v[108:111], v[132:133], off offset:2048
	global_load_dwordx4 v[112:115], v[132:133], off offset:3072
	v_add_co_u32_e32 v132, vcc, s12, v132
	s_nop 1
	v_addc_co_u32_e32 v133, vcc, 0, v133, vcc
	global_load_dwordx4 v[116:119], v[132:133], off
	global_load_dwordx4 v[120:123], v[132:133], off offset:1024
	global_load_dwordx4 v[124:127], v[132:133], off offset:2048
	global_load_dwordx4 v[128:131], v[132:133], off offset:3072
	v_max_f32_e64 v45, |v31|, |v31|
	s_waitcnt lgkmcnt(0)
	s_nop 0
	v_max_f32_e64 v46, |v30|, |v30|
	v_max_f32_e64 v47, |v27|, |v27|
	v_max_f32_e64 v48, |v26|, |v26|
	v_max_f32_e64 v49, |v23|, |v23|
	v_max_f32_e64 v50, |v22|, |v22|
	v_max_f32_e64 v51, |v19|, |v19|
	v_max_f32_e64 v52, |v18|, |v18|
	v_max_f32_e32 v45, v46, v45
	v_max_f32_e32 v46, v48, v47
	v_max_f32_e32 v47, v50, v49
	v_max_f32_e32 v48, v52, v51
	v_max3_f32 v45, |v28|, |v29|, v45
	v_max3_f32 v46, |v24|, |v25|, v46
	v_max3_f32 v47, |v20|, |v21|, v47
	v_max3_f32 v48, |v16|, |v17|, v48
	v_max3_f32 v45, v45, 0, v46
	v_max3_f32 v45, v45, v47, v48
	v_max_f32_e64 v49, |v15|, |v15|
	v_max_f32_e64 v50, |v14|, |v14|
	v_max_f32_e64 v51, |v11|, |v11|
	v_max_f32_e64 v52, |v10|, |v10|
	v_max_f32_e64 v53, |v7|, |v7|
	v_max_f32_e64 v54, |v6|, |v6|
	v_max_f32_e64 v55, |v3|, |v3|
	v_max_f32_e64 v56, |v2|, |v2|
	v_max_f32_e32 v49, v50, v49
	v_max_f32_e32 v50, v52, v51
	v_max_f32_e32 v51, v54, v53
	v_max_f32_e32 v52, v56, v55
	v_max3_f32 v46, |v12|, |v13|, v49
	v_max3_f32 v49, |v8|, |v9|, v50
	v_max3_f32 v50, |v4|, |v5|, v51
	v_max3_f32 v51, |v0|, |v1|, v52
	v_max3_f32 v45, v45, v46, v49
	v_max3_f32 v45, v45, v50, v51
	s_waitcnt lgkmcnt(0)
	s_nop 1
	v_max_f32_dpp v45, v45, v45 quad_perm:[1,0,3,2] row_mask:0xf bank_mask:0xf
	s_nop 1
	v_max_f32_dpp v45, v45, v45 quad_perm:[2,3,0,1] row_mask:0xf bank_mask:0xf
	s_nop 1
	v_max_f32_dpp v45, v45, v45 row_half_mirror row_mask:0xf bank_mask:0xf
	s_nop 1
	v_max_f32_dpp v45, v45, v45 row_mirror row_mask:0xf bank_mask:0xf
	s_nop 1
	v_max_f32_dpp v45, v45, v45 row_bcast:15 row_mask:0xa bank_mask:0xf
	s_nop 1
	v_max_f32_dpp v45, v45, v45 row_bcast:31 row_mask:0xc bank_mask:0xf
	s_nop 1
	v_readlane_b32 s100, v45, 63
	s_nop 3
	v_mov_b32_e32 v45, s100
	v_mov_b32_e32 v46, s100
	s_waitcnt lgkmcnt(0)
; #define GAS __attribute__((address_space(1)))
; __device__ __forceinline__ unsigned f2bf(float f) { unsigned u = __builtin_bit_cast(unsigned, f); return (u + 0x7fffu + ((u >> 16) & 1u)) >> 16; }
; __device__ __forceinline__ void row_to_fp4(const float* src, unsigned char* dst, size_t slice_stride, unsigned short* scale_out, int lane) {
;     ...
;     const float sc = mx > 0.f ? bf_lo(f2bf(mx * (1.0f / 6.0f)) ) : 1.0f, inv = 1.0f / sc;
; #pragma unroll
;     for (int q = 0; q < 8; ++q) { const f32x4 a = v[q] * inv;
;         unsigned w = 0u;
;         w = __builtin_amdgcn_cvt_scalef32_pk_fp4_f32(w, a[0], a[1], 1.0f, 0); w = __builtin_amdgcn_cvt_scalef32_pk_fp4_f32(w, a[2], a[3], 1.0f, 1);
;         *(GAS unsigned short*)(dst + (size_t)q * slice_stride + lane * 2) = (unsigned short)w; }
;     if (lane == 0) *(GAS unsigned short*)scale_out = (unsigned short)f2bf(sc);
; }
	v_max_f32_e32 v46, v46, v46
	v_max_f32_e32 v46, v45, v46
	v_cmp_lt_f32_e32 vcc, 0, v46
	v_mov_b32_e32 v45, 1.0
	s_and_saveexec_b64 s[8:9], vcc
	v_mul_f32_e32 v45, 0x3e2aaaab, v46
	v_bfe_u32 v46, v45, 16, 1
	v_add3_u32 v45, v45, v46, s13
	v_and_b32_e32 v45, 0xffff0000, v45
	s_or_b64 exec, exec, s[8:9]
	s_and_b64 s[8:9], s[2:3], exec
	s_cselect_b32 s8, s14, 0x3b400000
	s_add_u32 s22, s62, s8
	s_addc_u32 s23, s63, 0
	s_lshr_b32 s8, s7, 18
	s_add_i32 s24, s6, s8
	s_ashr_i32 s8, s24, 14
	s_ashr_i32 s9, s8, 31
	s_lshl_b64 s[8:9], s[8:9], 24
	s_add_u32 s25, s22, s8
	s_addc_u32 s26, s23, s9
	v_div_scale_f32 v46, s[22:23], v45, v45, 1.0
	v_rcp_f32_e32 v47, v46
	s_and_b32 s8, s24, 0xffffc000
	s_sub_i32 s8, s6, s8
	s_ashr_i32 s9, s8, 31
	v_fma_f32 v48, -v46, v47, 1.0
	v_fmac_f32_e32 v47, v48, v47
	v_div_scale_f32 v48, vcc, 1.0, v45, 1.0
	v_mul_f32_e32 v49, v48, v47
	v_fma_f32 v50, -v46, v49, v48
	v_fmac_f32_e32 v49, v50, v47
	v_fma_f32 v46, -v46, v49, v48
	v_div_fmas_f32 v46, v46, v47, v49
	v_div_fixup_f32 v46, v46, v45, 1.0
	s_lshl_b64 s[8:9], s[8:9], 7
	v_pk_mul_f32 v[30:31], v[30:31], v[46:47] op_sel_hi:[1,0]
	v_pk_mul_f32 v[28:29], v[28:29], v[46:47] op_sel_hi:[1,0]
	v_mov_b32_e32 v47, 0
	s_add_u32 s8, s25, s8
	v_cvt_scalef32_pk_fp4_f32 v47, v28, v29, 1.0
	s_addc_u32 s9, s26, s9
	v_cvt_scalef32_pk_fp4_f32 v47, v30, v31, 1.0 op_sel:[0,0,1,0]
	v_lshl_add_u64 v[48:49], s[8:9], 0, v[36:37]
	v_pk_mul_f32 v[24:25], v[24:25], v[46:47] op_sel_hi:[1,0]
	v_mov_b32_e32 v28, 0
	v_pk_mul_f32 v[26:27], v[26:27], v[46:47] op_sel_hi:[1,0]
	v_cvt_scalef32_pk_fp4_f32 v28, v24, v25, 1.0
	v_add_co_u32_e32 v24, vcc, s15, v48
	v_cvt_scalef32_pk_fp4_f32 v28, v26, v27, 1.0 op_sel:[0,0,1,0]
	s_nop 0
	v_addc_co_u32_e32 v25, vcc, 0, v49, vcc
	global_store_short v[24:25], v28, off
	v_pk_mul_f32 v[20:21], v[20:21], v[46:47] op_sel_hi:[1,0]
	v_mov_b32_e32 v24, 0
	v_pk_mul_f32 v[22:23], v[22:23], v[46:47] op_sel_hi:[1,0]
	v_cvt_scalef32_pk_fp4_f32 v24, v20, v21, 1.0
	v_add_co_u32_e32 v20, vcc, s16, v48
	v_cvt_scalef32_pk_fp4_f32 v24, v22, v23, 1.0 op_sel:[0,0,1,0]
	s_nop 0
	v_addc_co_u32_e32 v21, vcc, 0, v49, vcc
	global_store_short v[20:21], v24, off
	v_pk_mul_f32 v[16:17], v[16:17], v[46:47] op_sel_hi:[1,0]
	v_mov_b32_e32 v20, 0
	v_pk_mul_f32 v[18:19], v[18:19], v[46:47] op_sel_hi:[1,0]
	v_cvt_scalef32_pk_fp4_f32 v20, v16, v17, 1.0
	v_add_co_u32_e32 v16, vcc, s17, v48
	v_cvt_scalef32_pk_fp4_f32 v20, v18, v19, 1.0 op_sel:[0,0,1,0]
	s_nop 0
	v_addc_co_u32_e32 v17, vcc, 0, v49, vcc
	global_store_short v[16:17], v20, off
	v_pk_mul_f32 v[12:13], v[12:13], v[46:47] op_sel_hi:[1,0]
	v_mov_b32_e32 v16, 0
	v_pk_mul_f32 v[14:15], v[14:15], v[46:47] op_sel_hi:[1,0]
	v_cvt_scalef32_pk_fp4_f32 v16, v12, v13, 1.0
	v_add_co_u32_e32 v12, vcc, s18, v48
	v_cvt_scalef32_pk_fp4_f32 v16, v14, v15, 1.0 op_sel:[0,0,1,0]
	s_nop 0
	v_addc_co_u32_e32 v13, vcc, 0, v49, vcc
	global_store_short v[12:13], v16, off
	v_pk_mul_f32 v[8:9], v[8:9], v[46:47] op_sel_hi:[1,0]
	v_mov_b32_e32 v12, 0
	v_pk_mul_f32 v[10:11], v[10:11], v[46:47] op_sel_hi:[1,0]
	v_cvt_scalef32_pk_fp4_f32 v12, v8, v9, 1.0
	v_add_co_u32_e32 v8, vcc, s19, v48
	v_cvt_scalef32_pk_fp4_f32 v12, v10, v11, 1.0 op_sel:[0,0,1,0]
	s_nop 0
	v_addc_co_u32_e32 v9, vcc, 0, v49, vcc
	global_store_short v[8:9], v12, off
	v_pk_mul_f32 v[4:5], v[4:5], v[46:47] op_sel_hi:[1,0]
	v_mov_b32_e32 v8, 0
	v_pk_mul_f32 v[6:7], v[6:7], v[46:47] op_sel_hi:[1,0]
	v_cvt_scalef32_pk_fp4_f32 v8, v4, v5, 1.0
	v_add_co_u32_e32 v4, vcc, s20, v48
	v_cvt_scalef32_pk_fp4_f32 v8, v6, v7, 1.0 op_sel:[0,0,1,0]
	s_nop 0
	v_addc_co_u32_e32 v5, vcc, 0, v49, vcc
	global_store_short v[4:5], v8, off
	v_pk_mul_f32 v[0:1], v[0:1], v[46:47] op_sel_hi:[1,0]
	v_mov_b32_e32 v4, 0
	v_pk_mul_f32 v[2:3], v[2:3], v[46:47] op_sel_hi:[1,0]
	v_cvt_scalef32_pk_fp4_f32 v4, v0, v1, 1.0
	v_add_co_u32_e32 v0, vcc, 0xe00000, v48
	v_cvt_scalef32_pk_fp4_f32 v4, v2, v3, 1.0 op_sel:[0,0,1,0]
	s_nop 0
	v_addc_co_u32_e32 v1, vcc, 0, v49, vcc
	global_store_short v[48:49], v47, off
	global_store_short v[0:1], v4, off
	s_and_saveexec_b64 s[8:9], s[0:1]
	s_cbranch_execz .LBB0_146
	s_lshl_b64 s[6:7], s[6:7], 2
	s_add_u32 s6, s10, s6
	v_cndmask_b32_e64 v0, 0, 1, s[2:3]
	v_bfe_u32 v1, v45, 16, 1
	s_addc_u32 s7, s11, s7
	v_lshlrev_b32_e32 v0, 1, v0
	v_add3_u32 v1, v45, v1, s13
	global_store_short_d16_hi v0, v1, s[6:7]
	s_branch .LBB0_146
